# v24 + waves 4-7 only: sub-head-0 score accumulators of zero-start tiles initialised by MFMA C=0 instead of 32 VALU moves
# baseline (speedup 1.0000x reference)
.Lc_l1s0:
	s_waitcnt lgkmcnt(5)
	v_mfma_f32_32x32x16_bf16 v[144:159], v[236:239], v[180:183], v[144:159]
	ds_read_b128 v[248:251], v6
	ds_read_b128 v[236:239], v6 offset:8192
	s_waitcnt lgkmcnt(6)
	v_mfma_f32_32x32x16_bf16 v[160:175], v[208:211], v[180:183], v[160:175]
	v_add_u32_e32 v7, v0, v231
	s_waitcnt lgkmcnt(5)
	v_mfma_f32_32x32x16_bf16 v[144:159], v[2:5], v[184:187], v[144:159]
	s_waitcnt lgkmcnt(4)
	v_mfma_f32_32x32x16_bf16 v[160:175], v[8:11], v[184:187], v[160:175]
	s_waitcnt lgkmcnt(3)
	v_mfma_f32_32x32x16_bf16 v[144:159], v[12:15], v[188:191], v[144:159]
	s_waitcnt lgkmcnt(2)
	v_mfma_f32_32x32x16_bf16 v[160:175], v[244:247], v[188:191], v[160:175]
	ds_read_b128 v[244:247], v7
	s_nop 9
	v_exp_f32_e32 v6, v144
	v_exp_f32_e32 v3, v145
	v_exp_f32_e32 v10, v148
	v_exp_f32_e32 v11, v149
	v_exp_f32_e32 v12, v150
	v_exp_f32_e32 v148, v152
	v_exp_f32_e32 v150, v153
	v_exp_f32_e32 v156, v156
	v_exp_f32_e32 v157, v157
	v_exp_f32_e32 v5, v146
	v_exp_f32_e32 v152, v154
	v_exp_f32_e32 v158, v158
	v_exp_f32_e32 v8, v147
	v_exp_f32_e32 v13, v151
	v_exp_f32_e32 v154, v155
	v_exp_f32_e32 v159, v159
	v_exp_f32_e32 v2, v160
	v_exp_f32_e32 v144, v164
	v_exp_f32_e32 v149, v168
	v_exp_f32_e32 v160, v172
	v_exp_f32_e32 v4, v161
	v_exp_f32_e32 v145, v165
	v_exp_f32_e32 v151, v169
	v_exp_f32_e32 v161, v173
	v_add_f32_e32 v14, v6, v3
	v_add_f32_e32 v15, v10, v11
	v_add_f32_e32 v164, v148, v150
	v_add_f32_e32 v165, v156, v157
	v_exp_f32_e32 v7, v162
	v_exp_f32_e32 v146, v166
	v_exp_f32_e32 v153, v170
	v_exp_f32_e32 v162, v174
	v_add_f32_e32 v14, v5, v14
	v_add_f32_e32 v15, v12, v15
	v_add_f32_e32 v164, v152, v164
	v_add_f32_e32 v165, v158, v165
	v_exp_f32_e32 v9, v163
	v_exp_f32_e32 v147, v167
	v_exp_f32_e32 v155, v171
	v_exp_f32_e32 v163, v175
	v_add_f32_e32 v14, v8, v14
	v_add_f32_e32 v15, v13, v15
	v_add_f32_e32 v164, v154, v164
	v_add_f32_e32 v165, v159, v165
	v_add_f32_e32 v14, v2, v14
	v_add_f32_e32 v15, v144, v15
	v_add_f32_e32 v164, v149, v164
	v_add_f32_e32 v165, v160, v165
	v_add_f32_e32 v14, v4, v14
	v_add_f32_e32 v15, v145, v15
	v_add_f32_e32 v164, v151, v164
	v_add_f32_e32 v165, v161, v165
	v_add_f32_e32 v14, v7, v14
	v_add_f32_e32 v15, v146, v15
	v_add_f32_e32 v164, v153, v164
	v_add_f32_e32 v165, v162, v165
	v_add_f32_e32 v14, v9, v14
	v_add_f32_e32 v15, v147, v15
	v_add_f32_e32 v164, v155, v164
	v_add_f32_e32 v165, v163, v165
	v_add_f32_e32 v14, v14, v15
	v_add_f32_e32 v15, v164, v165
	v_add_f32_e32 v14, v14, v15
	v_mov_b32_e32 v15, v14
	v_cvt_pk_bf16_f32 v208, v6, v3
	v_cvt_pk_bf16_f32 v209, v5, v8
	v_cvt_pk_bf16_f32 v210, v10, v11
	v_cvt_pk_bf16_f32 v211, v12, v13
	v_cvt_pk_bf16_f32 v10, v148, v150
	v_cvt_pk_bf16_f32 v11, v152, v154
	v_cvt_pk_bf16_f32 v12, v156, v157
	v_cvt_pk_bf16_f32 v13, v158, v159
	v_cvt_pk_bf16_f32 v6, v2, v4
	v_cvt_pk_bf16_f32 v7, v7, v9
	v_cvt_pk_bf16_f32 v8, v144, v145
	v_cvt_pk_bf16_f32 v9, v146, v147
	v_cvt_pk_bf16_f32 v2, v149, v151
	v_cvt_pk_bf16_f32 v3, v153, v155
	v_cvt_pk_bf16_f32 v4, v160, v161
	v_cvt_pk_bf16_f32 v5, v162, v163
	v_permlane32_swap_b32_e32 v14, v15
	v_permlane32_swap_b32_e32 v208, v210
	v_permlane32_swap_b32_e32 v209, v211
	v_permlane32_swap_b32_e32 v10, v12
	v_permlane32_swap_b32_e32 v11, v13
	v_permlane32_swap_b32_e32 v6, v8
	v_permlane32_swap_b32_e32 v7, v9
	v_permlane32_swap_b32_e32 v2, v4
	v_permlane32_swap_b32_e32 v3, v5
	s_nop 15
	s_nop 15
	v_mov_b32_e32 v160, 0
	s_andn2_b64 vcc, exec, s[44:45]
	v_mov_b32_e32 v161, 0
	v_mov_b32_e32 v162, 0
	v_mov_b32_e32 v163, 0
	v_mov_b32_e32 v164, 0
	v_mov_b32_e32 v165, 0
	v_mov_b32_e32 v166, 0
	v_mov_b32_e32 v167, 0
	v_mov_b32_e32 v168, 0
	v_mov_b32_e32 v169, 0
	v_mov_b32_e32 v170, 0
	v_mov_b32_e32 v171, 0
	v_mov_b32_e32 v172, 0
	v_mov_b32_e32 v173, 0
	v_mov_b32_e32 v174, 0
	v_mov_b32_e32 v175, 0
	v_mov_b32_e32 v144, 0
	v_mov_b32_e32 v145, 0
	v_mov_b32_e32 v146, 0
	v_mov_b32_e32 v147, 0
	v_mov_b32_e32 v148, 0
	v_mov_b32_e32 v149, 0
	v_mov_b32_e32 v150, 0
	v_mov_b32_e32 v151, 0
	v_mov_b32_e32 v152, 0
	v_mov_b32_e32 v153, 0
	v_mov_b32_e32 v154, 0
	v_mov_b32_e32 v155, 0
	v_mov_b32_e32 v156, 0
	v_mov_b32_e32 v157, 0
	v_mov_b32_e32 v158, 0
	v_mov_b32_e32 v159, 0
	s_cbranch_vccnz .LBB0_200
	s_andn2_b64 vcc, exec, s[42:43]
	s_mov_b64 s[42:43], -1
	s_cbranch_vccnz .LBB0_198
	v_add_u32_e32 v144, 0x21780, v212
	v_add_u32_e32 v146, 0x21708, v212
	v_add_u32_e32 v147, 0x21788, v212
	v_add_u32_e32 v148, 0x21720, v212
	v_add_u32_e32 v149, 0x217a0, v212
	v_add_u32_e32 v150, 0x21728, v212
	v_add_u32_e32 v151, 0x217a8, v212
	v_add_u32_e32 v152, 0x21740, v212
	v_add_u32_e32 v153, 0x217c0, v212
	v_add_u32_e32 v154, 0x21748, v212
	v_add_u32_e32 v155, 0x217c8, v212
	v_add_u32_e32 v156, 0x21760, v212
	v_add_u32_e32 v157, 0x217e0, v212
	v_add_u32_e32 v158, 0x21768, v212
	v_add_u32_e32 v159, 0x217e8, v212
	ds_read2_b32 v[160:161], v213 offset1:1
	ds_read2_b32 v[144:145], v144 offset1:1
	ds_read2_b32 v[162:163], v146 offset1:1
	ds_read2_b32 v[146:147], v147 offset1:1
	ds_read2_b32 v[164:165], v148 offset1:1
	ds_read2_b32 v[148:149], v149 offset1:1
	ds_read2_b32 v[166:167], v150 offset1:1
	ds_read2_b32 v[150:151], v151 offset1:1
	ds_read2_b32 v[168:169], v152 offset1:1
	ds_read2_b32 v[152:153], v153 offset1:1
	ds_read2_b32 v[170:171], v154 offset1:1
	ds_read2_b32 v[154:155], v155 offset1:1
	ds_read2_b32 v[172:173], v156 offset1:1
	ds_read2_b32 v[156:157], v157 offset1:1
	ds_read2_b32 v[174:175], v158 offset1:1
	ds_read2_b32 v[158:159], v159 offset1:1
	s_mov_b64 s[42:43], 0
